# window units: exp/sum/cvt block and next-tile global loads moved ahead of QK, K-fragment reads 3 deep (same restructure as the NA units)
# speedup vs baseline: 1.0465x; 1.0002x over previous
.LBB0_640:
	s_add_i32 s26, s27, 2
	ds_read_b128 v[64:67], v166 offset:49152
	ds_read_b128 v[230:233], v168 offset:49152
	ds_read_b128 v[234:237], v166 offset:57344
	ds_read_b128 v[238:241], v168 offset:57344
	v_add_f32_e32 v144, 0, v191
	v_add_f32_e32 v144, v201, v144
	v_add_f32_e32 v144, v145, v144
	v_add_f32_e32 v144, v200, v144
	v_add_f32_e32 v144, v146, v144
	v_add_f32_e32 v144, v190, v144
	v_add_f32_e32 v144, v147, v144
	v_add_f32_e32 v144, v189, v144
	v_add_f32_e32 v144, v186, v144
	v_add_f32_e32 v144, v188, v144
	v_add_f32_e32 v144, v185, v144
	v_add_f32_e32 v144, v187, v144
	v_exp_f32_e32 v142, v142
	v_add_f32_e32 v144, v182, v144
	v_exp_f32_e32 v143, v143
	v_add_f32_e32 v144, v184, v144
	v_exp_f32_e32 v140, v140
	v_add_f32_e32 v144, v181, v144
	v_exp_f32_e32 v141, v141
	v_add_f32_e32 v144, v183, v144
	v_exp_f32_e32 v138, v138
	v_add_f32_e32 v144, v142, v144
	v_exp_f32_e32 v139, v139
	v_add_f32_e32 v144, v143, v144
	v_exp_f32_e32 v136, v136
	v_add_f32_e32 v144, v140, v144
	v_exp_f32_e32 v137, v137
	v_add_f32_e32 v144, v141, v144
	v_exp_f32_e32 v134, v134
	v_add_f32_e32 v144, v138, v144
	v_exp_f32_e32 v135, v135
	v_add_f32_e32 v144, v139, v144
	v_exp_f32_e32 v132, v132
	v_add_f32_e32 v144, v136, v144
	v_exp_f32_e32 v133, v133
	v_add_f32_e32 v144, v137, v144
	v_exp_f32_e32 v130, v130
	v_add_f32_e32 v144, v134, v144
	v_exp_f32_e32 v131, v131
	v_add_f32_e32 v144, v135, v144
	v_exp_f32_e32 v128, v128
	v_add_f32_e32 v144, v132, v144
	v_exp_f32_e32 v129, v129
	v_add_f32_e32 v144, v133, v144
	v_add_f32_e32 v144, v130, v144
	v_add_f32_e32 v144, v131, v144
	v_add_f32_e32 v144, v128, v144
	v_add_f32_e32 v179, v129, v144
	v_mov_b32_e32 v180, v179
	v_cvt_pk_bf16_f32 v144, v191, v201
	v_cvt_pk_bf16_f32 v145, v145, v200
	v_cvt_pk_bf16_f32 v146, v146, v190
	v_cvt_pk_bf16_f32 v147, v147, v189
	v_cvt_pk_bf16_f32 v186, v186, v188
	v_cvt_pk_bf16_f32 v187, v185, v187
	v_cvt_pk_bf16_f32 v188, v182, v184
	v_cvt_pk_bf16_f32 v189, v181, v183
	v_cvt_pk_bf16_f32 v182, v142, v143
	v_cvt_pk_bf16_f32 v183, v140, v141
	v_cvt_pk_bf16_f32 v184, v138, v139
	v_cvt_pk_bf16_f32 v185, v136, v137
	v_cvt_pk_bf16_f32 v200, v134, v135
	v_cvt_pk_bf16_f32 v201, v132, v133
	v_cvt_pk_bf16_f32 v202, v130, v131
	s_nop 0
	v_permlane32_swap_b32_e32 v179, v180
	v_permlane32_swap_b32_e32 v144, v146
	v_cvt_pk_bf16_f32 v203, v128, v129
	v_permlane32_swap_b32_e32 v200, v202
	v_permlane32_swap_b32_e32 v145, v147
	v_permlane32_swap_b32_e32 v186, v188
	v_permlane32_swap_b32_e32 v187, v189
	v_permlane32_swap_b32_e32 v182, v184
	v_permlane32_swap_b32_e32 v183, v185
	v_permlane32_swap_b32_e32 v201, v203
	s_add_i32 s2, s27, 3
	s_cmp_lt_i32 s2, s20
	s_cselect_b64 s[8:9], -1, 0
	s_and_b64 s[2:3], s[8:9], exec
	s_cselect_b32 s2, 0, s20
	s_cselect_b32 s3, s19, 0x4000
	s_lshl_b32 s2, s2, 6
	s_sub_i32 s2, s3, s2
	s_add_i32 s2, s25, s2
	s_mulk_i32 s2, 0x2400
	s_add_i32 s10, s2, 0xfff70000
	s_add_u32 s2, s21, s10
	s_addc_u32 s3, s22, 0
	s_add_u32 s10, s23, s10
	s_addc_u32 s11, s24, 0
	v_lshl_add_u64 v[128:129], s[10:11], 0, v[192:193]
	v_lshl_add_u64 v[132:133], s[10:11], 0, v[152:153]
	v_lshl_add_u64 v[136:137], s[2:3], 0, v[192:193]
	v_lshl_add_u64 v[140:141], s[2:3], 0, v[152:153]
	global_load_dwordx4 v[128:131], v[128:129], off
	s_nop 0
	global_load_dwordx4 v[132:135], v[132:133], off
	s_nop 0
	global_load_dwordx4 v[136:139], v[136:137], off
	s_nop 0
	global_load_dwordx4 v[140:143], v[140:141], off
	s_cmp_ge_i32 s26, s20
	s_waitcnt lgkmcnt(3)
	v_mfma_f32_32x32x16_bf16 v[80:95], v[64:67], v[124:127], 0
	s_waitcnt lgkmcnt(2)
	v_mfma_f32_32x32x16_bf16 v[80:95], v[230:233], v[120:123], v[80:95]
	ds_read_b128 v[230:233], v167 offset:49152
	s_waitcnt lgkmcnt(2)
	v_mfma_f32_32x32x16_bf16 v[64:79], v[234:237], v[124:127], 0
	ds_read_b128 v[234:237], v167 offset:57344
	s_waitcnt lgkmcnt(2)
	v_mfma_f32_32x32x16_bf16 v[64:79], v[238:241], v[120:123], v[64:79]
	ds_read_b128 v[238:241], v165 offset:49152
	s_waitcnt lgkmcnt(2)
	v_mfma_f32_32x32x16_bf16 v[80:95], v[230:233], v[116:119], v[80:95]
	ds_read_b128 v[230:233], v165 offset:57344
	s_waitcnt lgkmcnt(2)
	v_mfma_f32_32x32x16_bf16 v[64:79], v[234:237], v[116:119], v[64:79]
	ds_read_b128 v[234:237], v164 offset:49152
	s_waitcnt lgkmcnt(2)
	v_mfma_f32_32x32x16_bf16 v[80:95], v[238:241], v[112:115], v[80:95]
	ds_read_b128 v[238:241], v164 offset:57344
	s_waitcnt lgkmcnt(2)
	v_mfma_f32_32x32x16_bf16 v[64:79], v[230:233], v[112:115], v[64:79]
	ds_read_b128 v[230:233], v163 offset:49152
	s_waitcnt lgkmcnt(2)
	v_mfma_f32_32x32x16_bf16 v[80:95], v[234:237], v[108:111], v[80:95]
	ds_read_b128 v[234:237], v163 offset:57344
	s_waitcnt lgkmcnt(2)
	v_mfma_f32_32x32x16_bf16 v[64:79], v[238:241], v[108:111], v[64:79]
	ds_read_b128 v[238:241], v162 offset:49152
	s_waitcnt lgkmcnt(2)
	v_mfma_f32_32x32x16_bf16 v[80:95], v[230:233], v[104:107], v[80:95]
	ds_read_b128 v[230:233], v162 offset:57344
	s_waitcnt lgkmcnt(2)
	v_mfma_f32_32x32x16_bf16 v[64:79], v[234:237], v[104:107], v[64:79]
	ds_read_b128 v[234:237], v161 offset:49152
	s_waitcnt lgkmcnt(2)
	v_mfma_f32_32x32x16_bf16 v[80:95], v[238:241], v[100:103], v[80:95]
	ds_read_b128 v[238:241], v161 offset:57344
	s_waitcnt lgkmcnt(2)
	v_mfma_f32_32x32x16_bf16 v[64:79], v[230:233], v[100:103], v[64:79]
	s_waitcnt lgkmcnt(1)
	v_mfma_f32_32x32x16_bf16 v[80:95], v[234:237], v[96:99], v[80:95]
	s_waitcnt lgkmcnt(0)
	v_mfma_f32_32x32x16_bf16 v[64:79], v[238:241], v[96:99], v[64:79]
	s_cbranch_scc1 .LBB0_644
	s_add_i32 s2, s5, s25
	s_addk_i32 s2, 0xff00
	v_cmp_lt_i32_e32 vcc, s2, v175
	v_cmp_gt_i32_e64 s[2:3], s2, v176
	s_or_b64 s[8:9], vcc, s[2:3]
	s_and_saveexec_b64 s[2:3], s[8:9]
	s_cbranch_execz .LBB0_643
	v_add_u32_e32 v242, s25, v178
	v_add_u32_e32 v243, 0xffffff80, v242
	s_movk_i32 s8, 0x101
	v_cmp_gt_u32_e32 vcc, s8, v243
	v_add_u32_e32 v243, 0xffffffa0, v242
	s_nop 0
	v_cndmask_b32_e32 v80, v217, v80, vcc
	v_cmp_gt_u32_e32 vcc, s8, v243
	v_add_u32_e32 v243, 0xffffff81, v242
	s_nop 0
	v_cndmask_b32_e32 v64, v217, v64, vcc
	v_cmp_gt_u32_e32 vcc, s8, v243
	v_add_u32_e32 v243, 0xffffffa1, v242
	s_nop 0
	v_cndmask_b32_e32 v81, v217, v81, vcc
	v_cmp_gt_u32_e32 vcc, s8, v243
	v_add_u32_e32 v243, 0xffffff82, v242
	s_nop 0
	v_cndmask_b32_e32 v65, v217, v65, vcc
	v_cmp_gt_u32_e32 vcc, s8, v243
	v_add_u32_e32 v243, 0xffffffa2, v242
	s_nop 0
	v_cndmask_b32_e32 v82, v217, v82, vcc
	v_cmp_gt_u32_e32 vcc, s8, v243
	v_add_u32_e32 v243, 0xffffff83, v242
	s_nop 0
	v_cndmask_b32_e32 v66, v217, v66, vcc
	v_cmp_gt_u32_e32 vcc, s8, v243
	v_add_u32_e32 v243, 0xffffffa3, v242
	s_nop 0
	v_cndmask_b32_e32 v83, v217, v83, vcc
	v_cmp_gt_u32_e32 vcc, s8, v243
	v_add_u32_e32 v243, 0xffffff88, v242
	s_nop 0
	v_cndmask_b32_e32 v67, v217, v67, vcc
	v_cmp_gt_u32_e32 vcc, s8, v243
	v_add_u32_e32 v243, 0xffffffa8, v242
	s_nop 0
	v_cndmask_b32_e32 v84, v217, v84, vcc
	v_cmp_gt_u32_e32 vcc, s8, v243
	v_add_u32_e32 v243, 0xffffff89, v242
	s_nop 0
	v_cndmask_b32_e32 v68, v217, v68, vcc
	v_cmp_gt_u32_e32 vcc, s8, v243
	v_add_u32_e32 v243, 0xffffffa9, v242
	s_nop 0
	v_cndmask_b32_e32 v85, v217, v85, vcc
	v_cmp_gt_u32_e32 vcc, s8, v243
	v_add_u32_e32 v243, 0xffffff8a, v242
	s_nop 0
	v_cndmask_b32_e32 v69, v217, v69, vcc
	v_cmp_gt_u32_e32 vcc, s8, v243
	v_add_u32_e32 v243, 0xffffffaa, v242
	s_nop 0
	v_cndmask_b32_e32 v86, v217, v86, vcc
	v_cmp_gt_u32_e32 vcc, s8, v243
	v_add_u32_e32 v243, 0xffffff8b, v242
	s_nop 0
	v_cndmask_b32_e32 v70, v217, v70, vcc
	v_cmp_gt_u32_e32 vcc, s8, v243
	v_add_u32_e32 v243, 0xffffffab, v242
	s_nop 0
	v_cndmask_b32_e32 v87, v217, v87, vcc
	v_cmp_gt_u32_e32 vcc, s8, v243
	v_add_u32_e32 v243, 0xffffff90, v242
	s_nop 0
	v_cndmask_b32_e32 v71, v217, v71, vcc
	v_cmp_gt_u32_e32 vcc, s8, v243
	v_add_u32_e32 v243, 0xffffffb0, v242
	s_nop 0
	v_cndmask_b32_e32 v88, v217, v88, vcc
	v_cmp_gt_u32_e32 vcc, s8, v243
	v_add_u32_e32 v243, 0xffffff91, v242
	s_nop 0
	v_cndmask_b32_e32 v72, v217, v72, vcc
	v_cmp_gt_u32_e32 vcc, s8, v243
	v_add_u32_e32 v243, 0xffffffb1, v242
	s_nop 0
	v_cndmask_b32_e32 v89, v217, v89, vcc
	v_cmp_gt_u32_e32 vcc, s8, v243
	v_add_u32_e32 v243, 0xffffff92, v242
	s_nop 0
	v_cndmask_b32_e32 v73, v217, v73, vcc
	v_cmp_gt_u32_e32 vcc, s8, v243
	v_add_u32_e32 v243, 0xffffffb2, v242
	s_nop 0
	v_cndmask_b32_e32 v90, v217, v90, vcc
	v_cmp_gt_u32_e32 vcc, s8, v243
	v_add_u32_e32 v243, 0xffffff93, v242
	s_nop 0
	v_cndmask_b32_e32 v74, v217, v74, vcc
	v_cmp_gt_u32_e32 vcc, s8, v243
	v_add_u32_e32 v243, 0xffffffb3, v242
	s_nop 0
	v_cndmask_b32_e32 v91, v217, v91, vcc
	v_cmp_gt_u32_e32 vcc, s8, v243
	v_add_u32_e32 v243, 0xffffff98, v242
	s_nop 0
	v_cndmask_b32_e32 v75, v217, v75, vcc
	v_cmp_gt_u32_e32 vcc, s8, v243
	v_add_u32_e32 v243, 0xffffffb8, v242
	s_nop 0
	v_cndmask_b32_e32 v92, v217, v92, vcc
	v_cmp_gt_u32_e32 vcc, s8, v243
	v_add_u32_e32 v243, 0xffffff99, v242
	s_nop 0
	v_cndmask_b32_e32 v76, v217, v76, vcc
	v_cmp_gt_u32_e32 vcc, s8, v243
	v_add_u32_e32 v243, 0xffffffb9, v242
	s_nop 0
	v_cndmask_b32_e32 v93, v217, v93, vcc
	v_cmp_gt_u32_e32 vcc, s8, v243
	v_add_u32_e32 v243, 0xffffff9a, v242
	s_nop 0
	v_cndmask_b32_e32 v77, v217, v77, vcc
	v_cmp_gt_u32_e32 vcc, s8, v243
	v_add_u32_e32 v243, 0xffffffba, v242
	s_nop 0
	v_cndmask_b32_e32 v94, v217, v94, vcc
	v_cmp_gt_u32_e32 vcc, s8, v243
	v_add_u32_e32 v243, 0xffffff9b, v242
	v_add_u32_e32 v242, 0xffffffbb, v242
	v_cndmask_b32_e32 v78, v217, v78, vcc
	v_cmp_gt_u32_e32 vcc, s8, v243
	s_nop 1
	v_cndmask_b32_e32 v95, v217, v95, vcc
	v_cmp_gt_u32_e32 vcc, s8, v242
	s_nop 1
	v_cndmask_b32_e32 v79, v217, v79, vcc

.LBB0_644:
	s_add_i32 s2, s27, 3
	s_cmp_lt_i32 s2, s20
	s_cselect_b64 s[8:9], -1, 0
	ds_read_b64_tr_b16 v[204:205], v160 offset:0
	ds_read_b64_tr_b16 v[206:207], v160 offset:0x800
	ds_read_b64_tr_b16 v[208:209], v160 offset:0x1000
	ds_read_b64_tr_b16 v[210:211], v160 offset:0x1800
	ds_read_b64_tr_b16 v[212:213], v160 offset:0x2000
	ds_read_b64_tr_b16 v[214:215], v160 offset:0x2800
	ds_read_b64_tr_b16 v[218:219], v160 offset:0x3000
	ds_read_b64_tr_b16 v[220:221], v160 offset:0x3800
	s_waitcnt lgkmcnt(0)
	s_nop 0
	v_mfma_f32_32x32x16_bf16 v[48:63], v[144:147], v[204:207], v[48:63]
	ds_read_b64_tr_b16 v[204:205], v160 offset:0x200
	ds_read_b64_tr_b16 v[206:207], v160 offset:0xa00
	v_mfma_f32_32x32x16_bf16 v[48:63], v[186:189], v[208:211], v[48:63]
	ds_read_b64_tr_b16 v[208:209], v160 offset:0x1200
	ds_read_b64_tr_b16 v[210:211], v160 offset:0x1a00
	v_mfma_f32_32x32x16_bf16 v[48:63], v[182:185], v[212:215], v[48:63]
	ds_read_b64_tr_b16 v[212:213], v160 offset:0x2200
	ds_read_b64_tr_b16 v[214:215], v160 offset:0x2a00
	v_mfma_f32_32x32x16_bf16 v[48:63], v[200:203], v[218:221], v[48:63]
	ds_read_b64_tr_b16 v[218:219], v160 offset:0x3200
	ds_read_b64_tr_b16 v[220:221], v160 offset:0x3a00
	s_waitcnt lgkmcnt(0)
	v_mfma_f32_32x32x16_bf16 v[32:47], v[144:147], v[204:207], v[32:47]
	ds_read_b64_tr_b16 v[204:205], v160 offset:0x400
	ds_read_b64_tr_b16 v[206:207], v160 offset:0xc00
	v_mfma_f32_32x32x16_bf16 v[32:47], v[186:189], v[208:211], v[32:47]
	ds_read_b64_tr_b16 v[208:209], v160 offset:0x1400
	ds_read_b64_tr_b16 v[210:211], v160 offset:0x1c00
	v_mfma_f32_32x32x16_bf16 v[32:47], v[182:185], v[212:215], v[32:47]
	ds_read_b64_tr_b16 v[212:213], v160 offset:0x2400
	ds_read_b64_tr_b16 v[214:215], v160 offset:0x2c00
	v_mfma_f32_32x32x16_bf16 v[32:47], v[200:203], v[218:221], v[32:47]
	ds_read_b64_tr_b16 v[218:219], v160 offset:0x3400
	ds_read_b64_tr_b16 v[220:221], v160 offset:0x3c00
	s_waitcnt lgkmcnt(0)
	v_mfma_f32_32x32x16_bf16 v[16:31], v[144:147], v[204:207], v[16:31]
	ds_read_b64_tr_b16 v[204:205], v160 offset:0x600
	ds_read_b64_tr_b16 v[206:207], v160 offset:0xe00
	v_mfma_f32_32x32x16_bf16 v[16:31], v[186:189], v[208:211], v[16:31]
	ds_read_b64_tr_b16 v[208:209], v160 offset:0x1600
	ds_read_b64_tr_b16 v[210:211], v160 offset:0x1e00
	v_mfma_f32_32x32x16_bf16 v[16:31], v[182:185], v[212:215], v[16:31]
	ds_read_b64_tr_b16 v[212:213], v160 offset:0x2600
	ds_read_b64_tr_b16 v[214:215], v160 offset:0x2e00
	v_mfma_f32_32x32x16_bf16 v[16:31], v[200:203], v[218:221], v[16:31]
	ds_read_b64_tr_b16 v[218:219], v160 offset:0x3600
	ds_read_b64_tr_b16 v[220:221], v160 offset:0x3e00
	s_waitcnt lgkmcnt(0)
	v_mfma_f32_32x32x16_bf16 v[0:15], v[144:147], v[204:207], v[0:15]
	v_max_f32_e32 v144, v81, v81
	v_max_f32_e32 v145, v80, v80
	v_max_f32_e32 v144, v145, v144
	v_max3_f32 v144, v144, v82, v83
	v_max3_f32 v144, v144, v84, v85
	v_max3_f32 v144, v144, v86, v87
	v_max3_f32 v144, v144, v88, v89
	v_max3_f32 v144, v144, v90, v91
	v_max3_f32 v144, v144, v92, v93
	v_mfma_f32_32x32x16_bf16 v[0:15], v[186:189], v[208:211], v[0:15]
	v_max3_f32 v144, v144, v94, v95
	v_max3_f32 v144, v144, v64, v65
	v_max3_f32 v144, v144, v66, v67
	v_max3_f32 v144, v144, v68, v69
	v_max3_f32 v144, v144, v70, v71
	v_max3_f32 v144, v144, v72, v73
	v_max3_f32 v144, v144, v74, v75
	v_max3_f32 v144, v144, v76, v77
	v_mfma_f32_32x32x16_bf16 v[0:15], v[182:185], v[212:215], v[0:15]
	v_max3_f32 v144, v144, v78, v79
	v_mov_b32_e32 v145, v144
	s_nop 1
	v_permlane32_swap_b32_e32 v144, v145
	v_max_f32_e32 v145, v145, v145
	v_max_f32_e32 v144, v144, v144
	v_max_f32_e32 v144, v144, v145
	v_sub_f32_e32 v145, v144, v174
	s_mov_b32 s2, 0x42b504f3
	v_cmp_ge_f32_e32 vcc, s2, v145
	v_max_f32_e32 v145, v174, v174
	v_max_f32_e32 v144, v145, v144
	v_mfma_f32_32x32x16_bf16 v[0:15], v[200:203], v[218:221], v[0:15]
	v_sub_f32_e32 v145, v174, v144
	v_mul_f32_e32 v145, 0x3e0293ee, v145
	v_exp_f32_e32 v145, v145
	s_cmp_eq_u64 vcc, exec
	s_cselect_b64 s[2:3], -1, 0
	s_barrier
	s_waitcnt vmcnt(0)
	v_cndmask_b32_e64 v202, v145, 1.0, s[2:3]
	v_cmp_gt_f32_e32 vcc, 1.0, v202
	s_waitcnt vmcnt(3)
	ds_write_b128 v169, v[128:131]
	s_waitcnt vmcnt(2)
	ds_write_b128 v170, v[132:135]
	s_waitcnt vmcnt(1)
	ds_write_b128 v171, v[136:139] offset:32768
	s_waitcnt vmcnt(0)
	ds_write_b128 v172, v[140:143] offset:32768
	s_cbranch_vccz .LBB0_648
	s_and_saveexec_b64 s[10:11], s[0:1]
	ds_write_b32 v158, v202 offset:128
	s_or_b64 exec, exec, s[10:11]
	s_waitcnt lgkmcnt(0)
	v_add_u32_e32 v140, v151, v150
	ds_read_b128 v[128:131], v140 offset:224
	ds_read_b128 v[132:135], v140 offset:192
	ds_read_b128 v[136:139], v140 offset:160
	ds_read_b128 v[140:143], v140 offset:128
	s_waitcnt lgkmcnt(3)
	v_pk_mul_f32 v[60:61], v[60:61], v[128:129]
	s_waitcnt lgkmcnt(2)
	v_pk_mul_f32 v[56:57], v[56:57], v[132:133]
	s_waitcnt lgkmcnt(1)
	v_pk_mul_f32 v[52:53], v[52:53], v[136:137]
	v_pk_mul_f32 v[62:63], v[62:63], v[130:131]
	v_pk_mul_f32 v[58:59], v[58:59], v[134:135]
	v_pk_mul_f32 v[54:55], v[54:55], v[138:139]
	s_waitcnt lgkmcnt(0)
	v_pk_mul_f32 v[50:51], v[50:51], v[142:143]
	v_pk_mul_f32 v[48:49], v[48:49], v[140:141]
	v_pk_mul_f32 v[44:45], v[44:45], v[128:129]
	v_pk_mul_f32 v[40:41], v[40:41], v[132:133]
	v_pk_mul_f32 v[36:37], v[36:37], v[136:137]
	v_pk_mul_f32 v[46:47], v[46:47], v[130:131]
	v_pk_mul_f32 v[42:43], v[42:43], v[134:135]
	v_pk_mul_f32 v[38:39], v[38:39], v[138:139]
	v_pk_mul_f32 v[34:35], v[34:35], v[142:143]
	v_pk_mul_f32 v[32:33], v[32:33], v[140:141]
	v_pk_mul_f32 v[28:29], v[28:29], v[128:129]
	v_pk_mul_f32 v[24:25], v[24:25], v[132:133]
	v_pk_mul_f32 v[20:21], v[20:21], v[136:137]
	v_pk_mul_f32 v[30:31], v[30:31], v[130:131]
	v_pk_mul_f32 v[26:27], v[26:27], v[134:135]
	v_pk_mul_f32 v[22:23], v[22:23], v[138:139]
	v_pk_mul_f32 v[18:19], v[18:19], v[142:143]
	v_pk_mul_f32 v[16:17], v[16:17], v[140:141]
	v_pk_mul_f32 v[12:13], v[12:13], v[128:129]
	v_pk_mul_f32 v[8:9], v[8:9], v[132:133]
	v_pk_mul_f32 v[4:5], v[4:5], v[136:137]
	v_pk_mul_f32 v[14:15], v[14:15], v[130:131]
	v_pk_mul_f32 v[10:11], v[10:11], v[134:135]
	v_pk_mul_f32 v[6:7], v[6:7], v[138:139]
	v_pk_mul_f32 v[2:3], v[2:3], v[142:143]
	v_pk_mul_f32 v[0:1], v[0:1], v[140:141]
.LBB0_648:
	v_cndmask_b32_e64 v174, v144, v174, s[2:3]
	v_mul_f32_e32 v144, 0xbe0293ee, v174
	v_fmamk_f32 v80, v80, 0x3e0293ee, v144
	v_fmamk_f32 v81, v81, 0x3e0293ee, v144
	v_fmamk_f32 v82, v82, 0x3e0293ee, v144
	v_fmamk_f32 v83, v83, 0x3e0293ee, v144
	v_fmamk_f32 v84, v84, 0x3e0293ee, v144
	v_fmamk_f32 v85, v85, 0x3e0293ee, v144
	v_fmamk_f32 v86, v86, 0x3e0293ee, v144
	v_fmamk_f32 v87, v87, 0x3e0293ee, v144
	v_fmamk_f32 v88, v88, 0x3e0293ee, v144
	v_fmamk_f32 v89, v89, 0x3e0293ee, v144
	v_fmamk_f32 v90, v90, 0x3e0293ee, v144
	v_fmamk_f32 v91, v91, 0x3e0293ee, v144
	v_fmamk_f32 v92, v92, 0x3e0293ee, v144
	v_fmamk_f32 v93, v93, 0x3e0293ee, v144
	v_fmamk_f32 v94, v94, 0x3e0293ee, v144
	v_fmamk_f32 v95, v95, 0x3e0293ee, v144
	v_exp_f32_e32 v141, v80
	v_exp_f32_e32 v143, v81
	v_exp_f32_e32 v139, v82
	v_exp_f32_e32 v142, v83
	v_exp_f32_e32 v137, v84
	v_exp_f32_e32 v140, v85
	v_exp_f32_e32 v136, v86
	v_exp_f32_e32 v138, v87
	v_exp_f32_e32 v133, v88
	v_exp_f32_e32 v135, v89
	v_exp_f32_e32 v131, v90
	v_exp_f32_e32 v134, v91
	v_exp_f32_e32 v129, v92
	v_exp_f32_e32 v132, v93
	v_exp_f32_e32 v128, v94
	v_exp_f32_e32 v130, v95
	v_fmamk_f32 v145, v64, 0x3e0293ee, v144
	v_fmamk_f32 v146, v65, 0x3e0293ee, v144
	v_fmamk_f32 v147, v66, 0x3e0293ee, v144
	v_fmamk_f32 v181, v67, 0x3e0293ee, v144
	v_fmamk_f32 v182, v68, 0x3e0293ee, v144
	v_fmamk_f32 v183, v69, 0x3e0293ee, v144
	v_fmamk_f32 v184, v70, 0x3e0293ee, v144
	v_fmamk_f32 v185, v71, 0x3e0293ee, v144
	v_fmamk_f32 v186, v72, 0x3e0293ee, v144
	v_fmamk_f32 v187, v73, 0x3e0293ee, v144
	v_fmamk_f32 v188, v74, 0x3e0293ee, v144
	v_fmamk_f32 v189, v75, 0x3e0293ee, v144
	v_fmamk_f32 v190, v76, 0x3e0293ee, v144
	v_fmamk_f32 v191, v77, 0x3e0293ee, v144
	v_fmamk_f32 v200, v78, 0x3e0293ee, v144
	v_fmac_f32_e32 v144, 0x3e0293ee, v79
	s_waitcnt lgkmcnt(0)
	s_barrier
	ds_read_b128 v[64:67], v166 offset:32768
	ds_read_b128 v[230:233], v168 offset:32768
	ds_read_b128 v[234:237], v166 offset:40960
	ds_read_b128 v[238:241], v168 offset:40960
	s_andn2_b64 vcc, exec, s[8:9]
	v_exp_f32_e32 v215, v144
	v_add_f32_e32 v144, 0, v141
	v_add_f32_e32 v144, v143, v144
	v_add_f32_e32 v144, v139, v144
	v_add_f32_e32 v144, v142, v144
	v_add_f32_e32 v144, v137, v144
	v_add_f32_e32 v144, v140, v144
	v_add_f32_e32 v144, v136, v144
	v_add_f32_e32 v144, v138, v144
	v_add_f32_e32 v144, v133, v144
	v_add_f32_e32 v144, v135, v144
	v_add_f32_e32 v144, v131, v144
	v_add_f32_e32 v144, v134, v144
	v_exp_f32_e32 v201, v145
	v_add_f32_e32 v144, v129, v144
	v_exp_f32_e32 v205, v146
	v_add_f32_e32 v144, v132, v144
	v_exp_f32_e32 v206, v147
	v_add_f32_e32 v144, v128, v144
	v_exp_f32_e32 v181, v181
	v_add_f32_e32 v144, v130, v144
	v_exp_f32_e32 v207, v182
	v_add_f32_e32 v144, v201, v144
	v_exp_f32_e32 v208, v183
	v_add_f32_e32 v144, v205, v144
	v_exp_f32_e32 v209, v184
	v_add_f32_e32 v144, v206, v144
	v_exp_f32_e32 v210, v185
	v_add_f32_e32 v144, v181, v144
	v_exp_f32_e32 v211, v186
	v_add_f32_e32 v144, v207, v144
	v_exp_f32_e32 v212, v187
	v_add_f32_e32 v144, v208, v144
	v_exp_f32_e32 v213, v188
	v_add_f32_e32 v144, v209, v144
	v_exp_f32_e32 v214, v189
	v_add_f32_e32 v144, v210, v144
	v_exp_f32_e32 v190, v190
	v_add_f32_e32 v144, v211, v144
	v_exp_f32_e32 v191, v191
	v_add_f32_e32 v144, v212, v144
	v_exp_f32_e32 v200, v200
	v_add_f32_e32 v144, v213, v144
	v_add_f32_e32 v144, v214, v144
	v_add_f32_e32 v144, v190, v144
	v_add_f32_e32 v144, v191, v144
	v_add_f32_e32 v144, v200, v144
	v_add_f32_e32 v203, v215, v144
	v_mov_b32_e32 v204, v203
	v_cvt_pk_bf16_f32 v144, v141, v143
	v_cvt_pk_bf16_f32 v145, v139, v142
	v_cvt_pk_bf16_f32 v146, v137, v140
	v_cvt_pk_bf16_f32 v147, v136, v138
	s_nop 1
	v_permlane32_swap_b32_e32 v203, v204
	v_permlane32_swap_b32_e32 v144, v146
	v_permlane32_swap_b32_e32 v145, v147
	v_cvt_pk_bf16_f32 v182, v133, v135
	v_cvt_pk_bf16_f32 v183, v131, v134
	v_cvt_pk_bf16_f32 v184, v129, v132
	v_cvt_pk_bf16_f32 v185, v128, v130
	v_cvt_pk_bf16_f32 v186, v201, v205
	v_cvt_pk_bf16_f32 v187, v206, v181
	v_cvt_pk_bf16_f32 v188, v207, v208
	v_cvt_pk_bf16_f32 v189, v209, v210
	v_cvt_pk_bf16_f32 v206, v211, v212
	v_cvt_pk_bf16_f32 v207, v213, v214
	v_cvt_pk_bf16_f32 v208, v190, v191
	v_cvt_pk_bf16_f32 v209, v200, v215
	s_nop 0
	v_permlane32_swap_b32_e32 v182, v184
	v_permlane32_swap_b32_e32 v183, v185
	v_permlane32_swap_b32_e32 v186, v188
	v_permlane32_swap_b32_e32 v187, v189
	v_permlane32_swap_b32_e32 v206, v208
	v_permlane32_swap_b32_e32 v207, v209
	s_add_i32 s2, s27, 4
	s_cmp_lt_i32 s2, s20
	s_cselect_b32 s2, 0, s20
	s_cselect_b32 s3, s19, 0x4000
	s_lshl_b32 s2, s2, 6
	s_sub_i32 s2, s3, s2
	s_add_i32 s2, s25, s2
	s_mul_i32 s8, s2, 0x2400
	s_add_u32 s2, s21, s8
	s_addc_u32 s3, s22, 0
	s_add_u32 s8, s23, s8
	s_addc_u32 s9, s24, 0
	v_lshl_add_u64 v[128:129], s[8:9], 0, v[192:193]
	v_lshl_add_u64 v[132:133], s[8:9], 0, v[152:153]
	v_lshl_add_u64 v[136:137], s[2:3], 0, v[192:193]
	v_lshl_add_u64 v[140:141], s[2:3], 0, v[152:153]
	global_load_dwordx4 v[128:131], v[128:129], off
	s_nop 0
	global_load_dwordx4 v[132:135], v[132:133], off
	s_nop 0
	global_load_dwordx4 v[136:139], v[136:137], off
	s_nop 0
	global_load_dwordx4 v[140:143], v[140:141], off
	s_waitcnt lgkmcnt(3)
	v_mfma_f32_32x32x16_bf16 v[80:95], v[64:67], v[124:127], 0
	s_waitcnt lgkmcnt(2)
	v_mfma_f32_32x32x16_bf16 v[80:95], v[230:233], v[120:123], v[80:95]
	ds_read_b128 v[230:233], v167 offset:32768
	s_waitcnt lgkmcnt(2)
	v_mfma_f32_32x32x16_bf16 v[64:79], v[234:237], v[124:127], 0
	ds_read_b128 v[234:237], v167 offset:40960
	s_waitcnt lgkmcnt(2)
	v_mfma_f32_32x32x16_bf16 v[64:79], v[238:241], v[120:123], v[64:79]
	ds_read_b128 v[238:241], v165 offset:32768
	s_waitcnt lgkmcnt(2)
	v_mfma_f32_32x32x16_bf16 v[80:95], v[230:233], v[116:119], v[80:95]
	ds_read_b128 v[230:233], v165 offset:40960
	s_waitcnt lgkmcnt(2)
	v_mfma_f32_32x32x16_bf16 v[64:79], v[234:237], v[116:119], v[64:79]
	ds_read_b128 v[234:237], v164 offset:32768
	s_waitcnt lgkmcnt(2)
	v_mfma_f32_32x32x16_bf16 v[80:95], v[238:241], v[112:115], v[80:95]
	ds_read_b128 v[238:241], v164 offset:40960
	s_waitcnt lgkmcnt(2)
	v_mfma_f32_32x32x16_bf16 v[64:79], v[230:233], v[112:115], v[64:79]
	ds_read_b128 v[230:233], v163 offset:32768
	s_waitcnt lgkmcnt(2)
	v_mfma_f32_32x32x16_bf16 v[80:95], v[234:237], v[108:111], v[80:95]
	ds_read_b128 v[234:237], v163 offset:40960
	s_waitcnt lgkmcnt(2)
	v_mfma_f32_32x32x16_bf16 v[64:79], v[238:241], v[108:111], v[64:79]
	ds_read_b128 v[238:241], v162 offset:32768
	s_waitcnt lgkmcnt(2)
	v_mfma_f32_32x32x16_bf16 v[80:95], v[230:233], v[104:107], v[80:95]
	ds_read_b128 v[230:233], v162 offset:40960
	s_waitcnt lgkmcnt(2)
	v_mfma_f32_32x32x16_bf16 v[64:79], v[234:237], v[104:107], v[64:79]
	ds_read_b128 v[234:237], v161 offset:32768
	s_waitcnt lgkmcnt(2)
	v_mfma_f32_32x32x16_bf16 v[80:95], v[238:241], v[100:103], v[80:95]
	ds_read_b128 v[238:241], v161 offset:40960
	s_waitcnt lgkmcnt(2)
	v_mfma_f32_32x32x16_bf16 v[64:79], v[230:233], v[100:103], v[64:79]
	s_waitcnt lgkmcnt(1)
	v_mfma_f32_32x32x16_bf16 v[80:95], v[234:237], v[96:99], v[80:95]
	s_waitcnt lgkmcnt(0)
	v_mfma_f32_32x32x16_bf16 v[64:79], v[238:241], v[96:99], v[64:79]
	s_cbranch_vccnz .LBB0_652
	s_add_i32 s2, s5, s25
	s_addk_i32 s2, 0xff40
	v_cmp_lt_i32_e32 vcc, s2, v175
	v_cmp_gt_i32_e64 s[2:3], s2, v176
	s_or_b64 s[8:9], vcc, s[2:3]
	s_and_saveexec_b64 s[2:3], s[8:9]
	s_cbranch_execz .LBB0_651
	v_add_u32_e32 v242, s25, v178
	v_subrev_u32_e32 v243, 64, v242
	s_movk_i32 s8, 0x101
	v_cmp_gt_u32_e32 vcc, s8, v243
	v_subrev_u32_e32 v243, 32, v242
	s_nop 0
	v_cndmask_b32_e32 v80, v217, v80, vcc
	v_cmp_gt_u32_e32 vcc, s8, v243
	v_subrev_u32_e32 v243, 63, v242
	s_nop 0
	v_cndmask_b32_e32 v64, v217, v64, vcc
	v_cmp_gt_u32_e32 vcc, s8, v243
	v_subrev_u32_e32 v243, 31, v242
	s_nop 0
	v_cndmask_b32_e32 v81, v217, v81, vcc
	v_cmp_gt_u32_e32 vcc, s8, v243
	v_subrev_u32_e32 v243, 62, v242
	s_nop 0
	v_cndmask_b32_e32 v65, v217, v65, vcc
	v_cmp_gt_u32_e32 vcc, s8, v243
	v_subrev_u32_e32 v243, 30, v242
	s_nop 0
	v_cndmask_b32_e32 v82, v217, v82, vcc
	v_cmp_gt_u32_e32 vcc, s8, v243
	v_subrev_u32_e32 v243, 61, v242
	s_nop 0
	v_cndmask_b32_e32 v66, v217, v66, vcc
	v_cmp_gt_u32_e32 vcc, s8, v243
	v_subrev_u32_e32 v243, 29, v242
	s_nop 0
	v_cndmask_b32_e32 v83, v217, v83, vcc
	v_cmp_gt_u32_e32 vcc, s8, v243
	v_subrev_u32_e32 v243, 56, v242
	s_nop 0
	v_cndmask_b32_e32 v67, v217, v67, vcc
	v_cmp_gt_u32_e32 vcc, s8, v243
	v_subrev_u32_e32 v243, 24, v242
	s_nop 0
	v_cndmask_b32_e32 v84, v217, v84, vcc
	v_cmp_gt_u32_e32 vcc, s8, v243
	v_subrev_u32_e32 v243, 55, v242
	s_nop 0
	v_cndmask_b32_e32 v68, v217, v68, vcc
	v_cmp_gt_u32_e32 vcc, s8, v243
	v_subrev_u32_e32 v243, 23, v242
	s_nop 0
	v_cndmask_b32_e32 v85, v217, v85, vcc
	v_cmp_gt_u32_e32 vcc, s8, v243
	v_subrev_u32_e32 v243, 54, v242
	s_nop 0
	v_cndmask_b32_e32 v69, v217, v69, vcc
	v_cmp_gt_u32_e32 vcc, s8, v243
	v_subrev_u32_e32 v243, 22, v242
	s_nop 0
	v_cndmask_b32_e32 v86, v217, v86, vcc
	v_cmp_gt_u32_e32 vcc, s8, v243
	v_subrev_u32_e32 v243, 53, v242
	s_nop 0
	v_cndmask_b32_e32 v70, v217, v70, vcc
	v_cmp_gt_u32_e32 vcc, s8, v243
	v_subrev_u32_e32 v243, 21, v242
	s_nop 0
	v_cndmask_b32_e32 v87, v217, v87, vcc
	v_cmp_gt_u32_e32 vcc, s8, v243
	v_subrev_u32_e32 v243, 48, v242
	s_nop 0
	v_cndmask_b32_e32 v71, v217, v71, vcc
	v_cmp_gt_u32_e32 vcc, s8, v243
	v_add_u32_e32 v243, -16, v242
	s_nop 0
	v_cndmask_b32_e32 v88, v217, v88, vcc
	v_cmp_gt_u32_e32 vcc, s8, v243
	v_subrev_u32_e32 v243, 47, v242
	s_nop 0
	v_cndmask_b32_e32 v72, v217, v72, vcc
	v_cmp_gt_u32_e32 vcc, s8, v243
	v_add_u32_e32 v243, -15, v242
	s_nop 0
	v_cndmask_b32_e32 v89, v217, v89, vcc
	v_cmp_gt_u32_e32 vcc, s8, v243
	v_subrev_u32_e32 v243, 46, v242
	s_nop 0
	v_cndmask_b32_e32 v73, v217, v73, vcc
	v_cmp_gt_u32_e32 vcc, s8, v243
	v_add_u32_e32 v243, -14, v242
	s_nop 0
	v_cndmask_b32_e32 v90, v217, v90, vcc
	v_cmp_gt_u32_e32 vcc, s8, v243
	v_subrev_u32_e32 v243, 45, v242
	s_nop 0
	v_cndmask_b32_e32 v74, v217, v74, vcc
	v_cmp_gt_u32_e32 vcc, s8, v243
	v_add_u32_e32 v243, -13, v242
	s_nop 0
	v_cndmask_b32_e32 v91, v217, v91, vcc
	v_cmp_gt_u32_e32 vcc, s8, v243
	v_subrev_u32_e32 v243, 40, v242
	s_nop 0
	v_cndmask_b32_e32 v75, v217, v75, vcc
	v_cmp_gt_u32_e32 vcc, s8, v243
	v_add_u32_e32 v243, -8, v242
	s_nop 0
	v_cndmask_b32_e32 v92, v217, v92, vcc
	v_cmp_gt_u32_e32 vcc, s8, v243
	v_subrev_u32_e32 v243, 39, v242
	s_nop 0
	v_cndmask_b32_e32 v76, v217, v76, vcc
	v_cmp_gt_u32_e32 vcc, s8, v243
	v_add_u32_e32 v243, -7, v242
	s_nop 0
	v_cndmask_b32_e32 v93, v217, v93, vcc
	v_cmp_gt_u32_e32 vcc, s8, v243
	v_subrev_u32_e32 v243, 38, v242
	s_nop 0
	v_cndmask_b32_e32 v77, v217, v77, vcc
	v_cmp_gt_u32_e32 vcc, s8, v243
	v_add_u32_e32 v243, -6, v242
	s_nop 0
	v_cndmask_b32_e32 v94, v217, v94, vcc
	v_cmp_gt_u32_e32 vcc, s8, v243
	v_subrev_u32_e32 v243, 37, v242
	v_add_u32_e32 v242, -5, v242
	v_cndmask_b32_e32 v78, v217, v78, vcc
	v_cmp_gt_u32_e32 vcc, s8, v243
	s_nop 1
	v_cndmask_b32_e32 v95, v217, v95, vcc
	v_cmp_gt_u32_e32 vcc, s8, v242
	s_nop 1
	v_cndmask_b32_e32 v79, v217, v79, vcc

.LBB0_652:
	ds_read_b64_tr_b16 v[210:211], v177 offset:0
	ds_read_b64_tr_b16 v[212:213], v177 offset:0x800
	ds_read_b64_tr_b16 v[218:219], v177 offset:0x1000
	ds_read_b64_tr_b16 v[220:221], v177 offset:0x1800
	ds_read_b64_tr_b16 v[222:223], v177 offset:0x2000
	ds_read_b64_tr_b16 v[224:225], v177 offset:0x2800
	ds_read_b64_tr_b16 v[226:227], v177 offset:0x3000
	ds_read_b64_tr_b16 v[228:229], v177 offset:0x3800
	s_waitcnt lgkmcnt(0)
	s_nop 0
	v_mfma_f32_32x32x16_bf16 v[48:63], v[144:147], v[210:213], v[48:63]
	ds_read_b64_tr_b16 v[210:211], v177 offset:0x200
	ds_read_b64_tr_b16 v[212:213], v177 offset:0xa00
	v_mfma_f32_32x32x16_bf16 v[48:63], v[182:185], v[218:221], v[48:63]
	ds_read_b64_tr_b16 v[218:219], v177 offset:0x1200
	ds_read_b64_tr_b16 v[220:221], v177 offset:0x1a00
	v_mfma_f32_32x32x16_bf16 v[48:63], v[186:189], v[222:225], v[48:63]
	ds_read_b64_tr_b16 v[222:223], v177 offset:0x2200
	ds_read_b64_tr_b16 v[224:225], v177 offset:0x2a00
	v_mfma_f32_32x32x16_bf16 v[48:63], v[206:209], v[226:229], v[48:63]
	ds_read_b64_tr_b16 v[226:227], v177 offset:0x3200
	ds_read_b64_tr_b16 v[228:229], v177 offset:0x3a00
	s_waitcnt lgkmcnt(0)
	v_mfma_f32_32x32x16_bf16 v[32:47], v[144:147], v[210:213], v[32:47]
	ds_read_b64_tr_b16 v[210:211], v177 offset:0x400
	ds_read_b64_tr_b16 v[212:213], v177 offset:0xc00
	v_mfma_f32_32x32x16_bf16 v[32:47], v[182:185], v[218:221], v[32:47]
	ds_read_b64_tr_b16 v[218:219], v177 offset:0x1400
	ds_read_b64_tr_b16 v[220:221], v177 offset:0x1c00
	v_mfma_f32_32x32x16_bf16 v[32:47], v[186:189], v[222:225], v[32:47]
	ds_read_b64_tr_b16 v[222:223], v177 offset:0x2400
	ds_read_b64_tr_b16 v[224:225], v177 offset:0x2c00
	v_mfma_f32_32x32x16_bf16 v[32:47], v[206:209], v[226:229], v[32:47]
	ds_read_b64_tr_b16 v[226:227], v177 offset:0x3400
	ds_read_b64_tr_b16 v[228:229], v177 offset:0x3c00
	s_waitcnt lgkmcnt(0)
	v_mfma_f32_32x32x16_bf16 v[16:31], v[144:147], v[210:213], v[16:31]
	ds_read_b64_tr_b16 v[210:211], v177 offset:0x600
	ds_read_b64_tr_b16 v[212:213], v177 offset:0xe00
	v_mfma_f32_32x32x16_bf16 v[16:31], v[182:185], v[218:221], v[16:31]
	ds_read_b64_tr_b16 v[218:219], v177 offset:0x1600
	ds_read_b64_tr_b16 v[220:221], v177 offset:0x1e00
	v_mfma_f32_32x32x16_bf16 v[16:31], v[186:189], v[222:225], v[16:31]
	ds_read_b64_tr_b16 v[222:223], v177 offset:0x2600
	ds_read_b64_tr_b16 v[224:225], v177 offset:0x2e00
	v_mfma_f32_32x32x16_bf16 v[16:31], v[206:209], v[226:229], v[16:31]
	ds_read_b64_tr_b16 v[226:227], v177 offset:0x3600
	ds_read_b64_tr_b16 v[228:229], v177 offset:0x3e00
	s_waitcnt lgkmcnt(0)
	v_mfma_f32_32x32x16_bf16 v[0:15], v[144:147], v[210:213], v[0:15]
	v_max_f32_e32 v144, v81, v81
	v_max_f32_e32 v145, v80, v80
	v_max_f32_e32 v144, v145, v144
	v_max3_f32 v144, v144, v82, v83
	v_max3_f32 v144, v144, v84, v85
	v_max3_f32 v144, v144, v86, v87
	v_max3_f32 v144, v144, v88, v89
	v_max3_f32 v144, v144, v90, v91
	v_max3_f32 v144, v144, v92, v93
	v_mfma_f32_32x32x16_bf16 v[0:15], v[182:185], v[218:221], v[0:15]
	v_max3_f32 v144, v144, v94, v95
	v_max3_f32 v144, v144, v64, v65
	v_max3_f32 v144, v144, v66, v67
	v_max3_f32 v144, v144, v68, v69
	v_max3_f32 v144, v144, v70, v71
	v_max3_f32 v144, v144, v72, v73
	v_max3_f32 v144, v144, v74, v75
	v_max3_f32 v144, v144, v76, v77
	v_mfma_f32_32x32x16_bf16 v[0:15], v[186:189], v[222:225], v[0:15]
	v_max3_f32 v144, v144, v78, v79
	v_mov_b32_e32 v145, v144
	s_nop 1
	v_permlane32_swap_b32_e32 v144, v145
	v_max_f32_e32 v145, v145, v145
	v_max_f32_e32 v144, v144, v144
	v_max_f32_e32 v144, v144, v145
	v_sub_f32_e32 v145, v144, v174
	s_mov_b32 s2, 0x42b504f3
	v_cmp_ge_f32_e32 vcc, s2, v145
	v_max_f32_e32 v145, v174, v174
	v_max_f32_e32 v145, v145, v144
	v_mfma_f32_32x32x16_bf16 v[0:15], v[206:209], v[226:229], v[0:15]
	v_sub_f32_e32 v144, v174, v145
	v_mul_f32_e32 v144, 0x3e0293ee, v144
	v_exp_f32_e32 v144, v144
	s_cmp_eq_u64 vcc, exec
	s_cselect_b64 s[2:3], -1, 0
	s_barrier
	s_waitcnt vmcnt(0)
	v_cndmask_b32_e64 v144, v144, 1.0, s[2:3]
	v_cmp_gt_f32_e32 vcc, 1.0, v144
	s_waitcnt vmcnt(3)
	ds_write_b128 v169, v[128:131] offset:16384
	s_waitcnt vmcnt(2)
	ds_write_b128 v170, v[132:135] offset:16384
	s_waitcnt vmcnt(1)
	ds_write_b128 v171, v[136:139] offset:49152
	s_waitcnt vmcnt(0)
	ds_write_b128 v172, v[140:143] offset:49152
	s_cbranch_vccz .LBB0_656
	s_and_saveexec_b64 s[8:9], s[0:1]
	ds_write_b32 v158, v144 offset:128
	s_or_b64 exec, exec, s[8:9]
	s_waitcnt lgkmcnt(0)
	v_add_u32_e32 v140, v151, v150
	ds_read_b128 v[128:131], v140 offset:224
	ds_read_b128 v[132:135], v140 offset:192
	ds_read_b128 v[136:139], v140 offset:128
	ds_read_b128 v[140:143], v140 offset:160
	s_waitcnt lgkmcnt(3)
	v_pk_mul_f32 v[62:63], v[62:63], v[130:131]
	v_pk_mul_f32 v[60:61], v[60:61], v[128:129]
	s_waitcnt lgkmcnt(2)
	v_pk_mul_f32 v[58:59], v[58:59], v[134:135]
	v_pk_mul_f32 v[56:57], v[56:57], v[132:133]
	s_waitcnt lgkmcnt(0)
	v_pk_mul_f32 v[54:55], v[54:55], v[142:143]
	v_pk_mul_f32 v[52:53], v[52:53], v[140:141]
	v_pk_mul_f32 v[50:51], v[50:51], v[138:139]
	v_pk_mul_f32 v[48:49], v[48:49], v[136:137]
	v_pk_mul_f32 v[46:47], v[46:47], v[130:131]
	v_pk_mul_f32 v[44:45], v[44:45], v[128:129]
	v_pk_mul_f32 v[42:43], v[42:43], v[134:135]
	v_pk_mul_f32 v[40:41], v[40:41], v[132:133]
	v_pk_mul_f32 v[38:39], v[38:39], v[142:143]
	v_pk_mul_f32 v[36:37], v[36:37], v[140:141]
	v_pk_mul_f32 v[34:35], v[34:35], v[138:139]
	v_pk_mul_f32 v[32:33], v[32:33], v[136:137]
	v_pk_mul_f32 v[30:31], v[30:31], v[130:131]
	v_pk_mul_f32 v[28:29], v[28:29], v[128:129]
	v_pk_mul_f32 v[26:27], v[26:27], v[134:135]
	v_pk_mul_f32 v[24:25], v[24:25], v[132:133]
	v_pk_mul_f32 v[22:23], v[22:23], v[142:143]
	v_pk_mul_f32 v[20:21], v[20:21], v[140:141]
	v_pk_mul_f32 v[18:19], v[18:19], v[138:139]
	v_pk_mul_f32 v[16:17], v[16:17], v[136:137]
	v_pk_mul_f32 v[14:15], v[14:15], v[130:131]
	v_pk_mul_f32 v[12:13], v[12:13], v[128:129]
	v_pk_mul_f32 v[10:11], v[10:11], v[134:135]
	v_pk_mul_f32 v[8:9], v[8:9], v[132:133]
	v_pk_mul_f32 v[6:7], v[6:7], v[142:143]
	v_pk_mul_f32 v[4:5], v[4:5], v[140:141]
	v_pk_mul_f32 v[2:3], v[2:3], v[138:139]
	v_pk_mul_f32 v[0:1], v[0:1], v[136:137]
